# v23 (grid-barrier early L1 invalidate) + non-leader workgroups poll the cross-XCD generation word directly
# baseline (speedup 1.0000x reference)
.LBB0_87:
	s_or_b64 exec, exec, s[28:29]
	v_cvt_f32_u32_e32 v5, v3
	s_waitcnt vmcnt(0)
	buffer_inv sc1
	v_readfirstlane_b32 s4, v4
	v_sub_u32_e32 v4, 0, v3
	v_rcp_iflag_f32_e32 v5, v5
	v_add_u32_e32 v6, s4, v1
	v_mul_f32_e32 v5, 0x4f7ffffe, v5
	v_cvt_u32_f32_e32 v5, v5
	v_mul_lo_u32 v1, v4, v5
	v_mul_hi_u32 v1, v5, v1
	v_add_u32_e32 v1, v5, v1
	v_mul_hi_u32 v1, v6, v1
	v_mul_lo_u32 v4, v1, v3
	v_sub_u32_e32 v4, v6, v4
	v_add_u32_e32 v5, 1, v1
	v_cmp_ge_u32_e32 vcc, v4, v3
	s_nop 1
	v_cndmask_b32_e32 v1, v1, v5, vcc
	v_sub_u32_e32 v5, v4, v3
	v_cndmask_b32_e32 v4, v4, v5, vcc
	v_add_u32_e32 v5, 1, v1
	v_cmp_ge_u32_e32 vcc, v4, v3
	v_add_u32_e32 v4, 1, v6
	s_nop 0
	v_cndmask_b32_e32 v1, v1, v5, vcc
	v_mul_lo_u32 v5, v3, v1
	v_add_u32_e32 v3, v5, v3
	v_cmp_ne_u32_e32 vcc, v4, v3
	s_and_saveexec_b64 s[4:5], vcc
	s_xor_b64 s[28:29], exec, s[4:5]
	s_cbranch_execz .LBB0_101
	v_readlane_b32 s4, v254, 49
	v_readlane_b32 s5, v254, 50
	s_waitcnt lgkmcnt(0)
	s_nop 3
	global_load_dword v2, v115, s[4:5] sc1
	s_waitcnt vmcnt(0)
	v_cmp_eq_u32_e32 vcc, v2, v1
	s_and_saveexec_b64 s[38:39], vcc
	s_cbranch_execz .LBB0_100
	s_mov_b32 s4, 1
	s_mov_b64 s[40:41], 0
	s_branch .LBB0_91

.LBB0_238:
	s_or_b64 exec, exec, s[26:27]
	v_cvt_f32_u32_e32 v5, v3
	s_waitcnt vmcnt(0)
	buffer_inv sc1
	v_readfirstlane_b32 s4, v4
	v_sub_u32_e32 v4, 0, v3
	v_rcp_iflag_f32_e32 v5, v5
	v_add_u32_e32 v6, s4, v1
	v_mul_f32_e32 v5, 0x4f7ffffe, v5
	v_cvt_u32_f32_e32 v5, v5
	v_mul_lo_u32 v1, v4, v5
	v_mul_hi_u32 v1, v5, v1
	v_add_u32_e32 v1, v5, v1
	v_mul_hi_u32 v1, v6, v1
	v_mul_lo_u32 v4, v1, v3
	v_sub_u32_e32 v4, v6, v4
	v_add_u32_e32 v5, 1, v1
	v_cmp_ge_u32_e32 vcc, v4, v3
	s_nop 1
	v_cndmask_b32_e32 v1, v1, v5, vcc
	v_sub_u32_e32 v5, v4, v3
	v_cndmask_b32_e32 v4, v4, v5, vcc
	v_add_u32_e32 v5, 1, v1
	v_cmp_ge_u32_e32 vcc, v4, v3
	v_add_u32_e32 v4, 1, v6
	s_nop 0
	v_cndmask_b32_e32 v1, v1, v5, vcc
	v_mul_lo_u32 v5, v3, v1
	v_add_u32_e32 v3, v5, v3
	v_cmp_ne_u32_e32 vcc, v4, v3
	s_and_saveexec_b64 s[4:5], vcc
	s_xor_b64 s[26:27], exec, s[4:5]
	s_cbranch_execz .LBB0_252
	v_readlane_b32 s4, v254, 49
	v_readlane_b32 s5, v254, 50
	s_waitcnt lgkmcnt(0)
	s_nop 3
	global_load_dword v2, v115, s[4:5] sc1
	s_waitcnt vmcnt(0)
	v_cmp_eq_u32_e32 vcc, v2, v1
	s_and_saveexec_b64 s[28:29], vcc
	s_cbranch_execz .LBB0_251
	s_mov_b32 s4, 1
	s_mov_b64 s[38:39], 0
	s_branch .LBB0_242

.LBB0_413:
	s_or_b64 exec, exec, s[10:11]
	v_cvt_f32_u32_e32 v5, v3
	s_waitcnt vmcnt(0)
	buffer_inv sc1
	v_readfirstlane_b32 s4, v4
	v_sub_u32_e32 v4, 0, v3
	v_rcp_iflag_f32_e32 v5, v5
	v_add_u32_e32 v6, s4, v1
	v_mul_f32_e32 v5, 0x4f7ffffe, v5
	v_cvt_u32_f32_e32 v5, v5
	v_mul_lo_u32 v1, v4, v5
	v_mul_hi_u32 v1, v5, v1
	v_add_u32_e32 v1, v5, v1
	v_mul_hi_u32 v1, v6, v1
	v_mul_lo_u32 v4, v1, v3
	v_sub_u32_e32 v4, v6, v4
	v_add_u32_e32 v5, 1, v1
	v_cmp_ge_u32_e32 vcc, v4, v3
	s_nop 1
	v_cndmask_b32_e32 v1, v1, v5, vcc
	v_sub_u32_e32 v5, v4, v3
	v_cndmask_b32_e32 v4, v4, v5, vcc
	v_add_u32_e32 v5, 1, v1
	v_cmp_ge_u32_e32 vcc, v4, v3
	v_add_u32_e32 v4, 1, v6
	s_nop 0
	v_cndmask_b32_e32 v1, v1, v5, vcc
	v_mul_lo_u32 v5, v3, v1
	v_add_u32_e32 v3, v5, v3
	v_cmp_ne_u32_e32 vcc, v4, v3
	s_and_saveexec_b64 s[4:5], vcc
	s_xor_b64 s[10:11], exec, s[4:5]
	s_cbranch_execz .LBB0_427
	v_readlane_b32 s4, v254, 49
	v_readlane_b32 s5, v254, 50
	s_waitcnt lgkmcnt(0)
	s_nop 3
	global_load_dword v2, v115, s[4:5] sc1
	s_waitcnt vmcnt(0)
	v_cmp_eq_u32_e32 vcc, v2, v1
	s_and_saveexec_b64 s[26:27], vcc
	s_cbranch_execz .LBB0_426
	s_mov_b32 s4, 1
	s_mov_b64 s[28:29], 0
	s_branch .LBB0_417

.LBB0_569:
	s_or_b64 exec, exec, s[10:11]
	v_cvt_f32_u32_e32 v5, v3
	s_waitcnt vmcnt(0)
	buffer_inv sc1
	v_readfirstlane_b32 s4, v4
	v_sub_u32_e32 v4, 0, v3
	v_rcp_iflag_f32_e32 v5, v5
	v_add_u32_e32 v6, s4, v1
	v_mul_f32_e32 v5, 0x4f7ffffe, v5
	v_cvt_u32_f32_e32 v5, v5
	v_mul_lo_u32 v1, v4, v5
	v_mul_hi_u32 v1, v5, v1
	v_add_u32_e32 v1, v5, v1
	v_mul_hi_u32 v1, v6, v1
	v_mul_lo_u32 v4, v1, v3
	v_sub_u32_e32 v4, v6, v4
	v_add_u32_e32 v5, 1, v1
	v_cmp_ge_u32_e32 vcc, v4, v3
	s_nop 1
	v_cndmask_b32_e32 v1, v1, v5, vcc
	v_sub_u32_e32 v5, v4, v3
	v_cndmask_b32_e32 v4, v4, v5, vcc
	v_add_u32_e32 v5, 1, v1
	v_cmp_ge_u32_e32 vcc, v4, v3
	v_add_u32_e32 v4, 1, v6
	s_nop 0
	v_cndmask_b32_e32 v1, v1, v5, vcc
	v_mul_lo_u32 v5, v3, v1
	v_add_u32_e32 v3, v5, v3
	v_cmp_ne_u32_e32 vcc, v4, v3
	s_and_saveexec_b64 s[4:5], vcc
	s_xor_b64 s[10:11], exec, s[4:5]
	s_cbranch_execz .LBB0_583
	v_readlane_b32 s4, v254, 49
	v_readlane_b32 s5, v254, 50
	s_waitcnt lgkmcnt(0)
	s_nop 3
	global_load_dword v2, v115, s[4:5] sc1
	s_waitcnt vmcnt(0)
	v_cmp_eq_u32_e32 vcc, v2, v1
	s_and_saveexec_b64 s[28:29], vcc
	s_cbranch_execz .LBB0_582
	s_mov_b32 s4, 1
	s_mov_b64 s[38:39], 0
	s_branch .LBB0_573

.LBB0_1021:
	s_or_b64 exec, exec, s[4:5]
	v_cvt_f32_u32_e32 v5, v3
	s_waitcnt vmcnt(0)
	buffer_inv sc1
	v_readfirstlane_b32 s4, v4
	v_sub_u32_e32 v4, 0, v3
	v_rcp_iflag_f32_e32 v5, v5
	v_add_u32_e32 v6, s4, v1
	v_mul_f32_e32 v5, 0x4f7ffffe, v5
	v_cvt_u32_f32_e32 v5, v5
	v_mul_lo_u32 v1, v4, v5
	v_mul_hi_u32 v1, v5, v1
	v_add_u32_e32 v1, v5, v1
	v_mul_hi_u32 v1, v6, v1
	v_mul_lo_u32 v4, v1, v3
	v_sub_u32_e32 v4, v6, v4
	v_add_u32_e32 v5, 1, v1
	v_cmp_ge_u32_e32 vcc, v4, v3
	s_nop 1
	v_cndmask_b32_e32 v1, v1, v5, vcc
	v_sub_u32_e32 v5, v4, v3
	v_cndmask_b32_e32 v4, v4, v5, vcc
	v_add_u32_e32 v5, 1, v1
	v_cmp_ge_u32_e32 vcc, v4, v3
	v_add_u32_e32 v4, 1, v6
	s_nop 0
	v_cndmask_b32_e32 v1, v1, v5, vcc
	v_mul_lo_u32 v5, v3, v1
	v_add_u32_e32 v3, v5, v3
	v_cmp_ne_u32_e32 vcc, v4, v3
	s_and_saveexec_b64 s[4:5], vcc
	s_xor_b64 s[4:5], exec, s[4:5]
	s_cbranch_execz .LBB0_1035
	v_readlane_b32 s8, v254, 49
	v_readlane_b32 s9, v254, 50
	s_waitcnt lgkmcnt(0)
	s_nop 3
	global_load_dword v2, v115, s[8:9] sc1
	s_waitcnt vmcnt(0)
	v_cmp_eq_u32_e32 vcc, v2, v1
	s_and_saveexec_b64 s[8:9], vcc
	s_cbranch_execz .LBB0_1034
	s_mov_b32 s7, 1
	s_mov_b64 s[10:11], 0
	s_branch .LBB0_1025

.LBB0_1124:
	s_or_b64 exec, exec, s[8:9]
	v_cvt_f32_u32_e32 v5, v3
	s_waitcnt vmcnt(0)
	buffer_inv sc1
	v_readfirstlane_b32 s7, v4
	v_sub_u32_e32 v4, 0, v3
	v_rcp_iflag_f32_e32 v5, v5
	v_add_u32_e32 v6, s7, v1
	v_mul_f32_e32 v5, 0x4f7ffffe, v5
	v_cvt_u32_f32_e32 v5, v5
	v_mul_lo_u32 v1, v4, v5
	v_mul_hi_u32 v1, v5, v1
	v_add_u32_e32 v1, v5, v1
	v_mul_hi_u32 v1, v6, v1
	v_mul_lo_u32 v4, v1, v3
	v_sub_u32_e32 v4, v6, v4
	v_add_u32_e32 v5, 1, v1
	v_cmp_ge_u32_e32 vcc, v4, v3
	s_nop 1
	v_cndmask_b32_e32 v1, v1, v5, vcc
	v_sub_u32_e32 v5, v4, v3
	v_cndmask_b32_e32 v4, v4, v5, vcc
	v_add_u32_e32 v5, 1, v1
	v_cmp_ge_u32_e32 vcc, v4, v3
	v_add_u32_e32 v4, 1, v6
	s_nop 0
	v_cndmask_b32_e32 v1, v1, v5, vcc
	v_mul_lo_u32 v5, v3, v1
	v_add_u32_e32 v3, v5, v3
	v_cmp_ne_u32_e32 vcc, v4, v3
	s_and_saveexec_b64 s[8:9], vcc
	s_xor_b64 s[8:9], exec, s[8:9]
	s_cbranch_execz .LBB0_1138
	v_readlane_b32 s10, v254, 49
	v_readlane_b32 s11, v254, 50
	s_waitcnt lgkmcnt(0)
	s_nop 3
	global_load_dword v2, v115, s[10:11] sc1
	s_waitcnt vmcnt(0)
	v_cmp_eq_u32_e32 vcc, v2, v1
	s_and_saveexec_b64 s[10:11], vcc
	s_cbranch_execz .LBB0_1137
	s_mov_b32 s7, 1
	s_mov_b64 s[26:27], 0
	s_branch .LBB0_1128
